# E28: E25 + NSA top-k rank sequence re-issued without the 64 hazard nops (two alternating readlane SGPRs, alternating vcc / SGPR-pair compare results, VOP3 add-with-carry) - same integer rank
# baseline (speedup 1.0000x reference)
.LBB0_677:
	v_mov_b32_e32 v69, v162
	s_and_saveexec_b64 s[0:1], s[16:17]
	ds_read_b32 v69, v68
	s_or_b64 exec, exec, s[0:1]
	s_waitcnt lgkmcnt(0)
	v_and_b32_e32 v0, 0xffffffc0, v69
	v_add_u32_e32 v0, 64, v0
	v_cmp_ngt_f32_e32 vcc, 0, v69
	s_nop 1
	v_cndmask_b32_e32 v0, 0, v0, vcc
	v_bitop3_b32 v0, v0, 63, v1 bitop3:0x36
	s_nop 0
	v_readlane_b32 s0, v0, 0
	v_readlane_b32 s1, v0, 1
	v_mov_b32_e32 v69, 0
	v_cmp_gt_i32_e32 vcc, s0, v0
	v_readlane_b32 s0, v0, 2
	v_cmp_gt_i32_e64 s[98:99], s1, v0
	v_readlane_b32 s1, v0, 3
	v_cndmask_b32_e64 v70, 0, 1, vcc
	v_addc_co_u32_e64 v69, s[2:3], v69, v70, s[98:99]
	v_cmp_gt_i32_e32 vcc, s0, v0
	v_readlane_b32 s0, v0, 4
	v_cmp_gt_i32_e64 s[98:99], s1, v0
	v_readlane_b32 s1, v0, 5
	v_cndmask_b32_e64 v70, 0, 1, vcc
	v_addc_co_u32_e64 v69, s[2:3], v69, v70, s[98:99]
	v_cmp_gt_i32_e32 vcc, s0, v0
	v_readlane_b32 s0, v0, 6
	v_cmp_gt_i32_e64 s[98:99], s1, v0
	v_readlane_b32 s1, v0, 7
	v_cndmask_b32_e64 v70, 0, 1, vcc
	v_addc_co_u32_e64 v69, s[2:3], v69, v70, s[98:99]
	v_cmp_gt_i32_e32 vcc, s0, v0
	v_readlane_b32 s0, v0, 8
	v_cmp_gt_i32_e64 s[98:99], s1, v0
	v_readlane_b32 s1, v0, 9
	v_cndmask_b32_e64 v70, 0, 1, vcc
	v_addc_co_u32_e64 v69, s[2:3], v69, v70, s[98:99]
	v_cmp_gt_i32_e32 vcc, s0, v0
	v_readlane_b32 s0, v0, 10
	v_cmp_gt_i32_e64 s[98:99], s1, v0
	v_readlane_b32 s1, v0, 11
	v_cndmask_b32_e64 v70, 0, 1, vcc
	v_addc_co_u32_e64 v69, s[2:3], v69, v70, s[98:99]
	v_cmp_gt_i32_e32 vcc, s0, v0
	v_readlane_b32 s0, v0, 12
	v_cmp_gt_i32_e64 s[98:99], s1, v0
	v_readlane_b32 s1, v0, 13
	v_cndmask_b32_e64 v70, 0, 1, vcc
	v_addc_co_u32_e64 v69, s[2:3], v69, v70, s[98:99]
	v_cmp_gt_i32_e32 vcc, s0, v0
	v_readlane_b32 s0, v0, 14
	v_cmp_gt_i32_e64 s[98:99], s1, v0
	v_readlane_b32 s1, v0, 15
	v_cndmask_b32_e64 v70, 0, 1, vcc
	v_addc_co_u32_e64 v69, s[2:3], v69, v70, s[98:99]
	v_cmp_gt_i32_e32 vcc, s0, v0
	v_readlane_b32 s0, v0, 16
	v_cmp_gt_i32_e64 s[98:99], s1, v0
	v_readlane_b32 s1, v0, 17
	v_cndmask_b32_e64 v70, 0, 1, vcc
	v_addc_co_u32_e64 v69, s[2:3], v69, v70, s[98:99]
	v_cmp_gt_i32_e32 vcc, s0, v0
	v_readlane_b32 s0, v0, 18
	v_cmp_gt_i32_e64 s[98:99], s1, v0
	v_readlane_b32 s1, v0, 19
	v_cndmask_b32_e64 v70, 0, 1, vcc
	v_addc_co_u32_e64 v69, s[2:3], v69, v70, s[98:99]
	v_cmp_gt_i32_e32 vcc, s0, v0
	v_readlane_b32 s0, v0, 20
	v_cmp_gt_i32_e64 s[98:99], s1, v0
	v_readlane_b32 s1, v0, 21
	v_cndmask_b32_e64 v70, 0, 1, vcc
	v_addc_co_u32_e64 v69, s[2:3], v69, v70, s[98:99]
	v_cmp_gt_i32_e32 vcc, s0, v0
	v_readlane_b32 s0, v0, 22
	v_cmp_gt_i32_e64 s[98:99], s1, v0
	v_readlane_b32 s1, v0, 23
	v_cndmask_b32_e64 v70, 0, 1, vcc
	v_addc_co_u32_e64 v69, s[2:3], v69, v70, s[98:99]
	v_cmp_gt_i32_e32 vcc, s0, v0
	v_readlane_b32 s0, v0, 24
	v_cmp_gt_i32_e64 s[98:99], s1, v0
	v_readlane_b32 s1, v0, 25
	v_cndmask_b32_e64 v70, 0, 1, vcc
	v_addc_co_u32_e64 v69, s[2:3], v69, v70, s[98:99]
	v_cmp_gt_i32_e32 vcc, s0, v0
	v_readlane_b32 s0, v0, 26
	v_cmp_gt_i32_e64 s[98:99], s1, v0
	v_readlane_b32 s1, v0, 27
	v_cndmask_b32_e64 v70, 0, 1, vcc
	v_addc_co_u32_e64 v69, s[2:3], v69, v70, s[98:99]
	v_cmp_gt_i32_e32 vcc, s0, v0
	v_readlane_b32 s0, v0, 28
	v_cmp_gt_i32_e64 s[98:99], s1, v0
	v_readlane_b32 s1, v0, 29
	v_cndmask_b32_e64 v70, 0, 1, vcc
	v_addc_co_u32_e64 v69, s[2:3], v69, v70, s[98:99]
	v_cmp_gt_i32_e32 vcc, s0, v0
	v_readlane_b32 s0, v0, 30
	v_cmp_gt_i32_e64 s[98:99], s1, v0
	v_readlane_b32 s1, v0, 31
	v_cndmask_b32_e64 v70, 0, 1, vcc
	v_addc_co_u32_e64 v69, s[2:3], v69, v70, s[98:99]
	v_cmp_gt_i32_e32 vcc, s0, v0
	v_readlane_b32 s0, v0, 32
	v_cmp_gt_i32_e64 s[98:99], s1, v0
	v_readlane_b32 s1, v0, 33
	v_cndmask_b32_e64 v70, 0, 1, vcc
	v_addc_co_u32_e64 v69, s[2:3], v69, v70, s[98:99]
	v_cmp_gt_i32_e32 vcc, s0, v0
	v_readlane_b32 s0, v0, 34
	v_cmp_gt_i32_e64 s[98:99], s1, v0
	v_readlane_b32 s1, v0, 35
	v_cndmask_b32_e64 v70, 0, 1, vcc
	v_addc_co_u32_e64 v69, s[2:3], v69, v70, s[98:99]
	v_cmp_gt_i32_e32 vcc, s0, v0
	v_readlane_b32 s0, v0, 36
	v_cmp_gt_i32_e64 s[98:99], s1, v0
	v_readlane_b32 s1, v0, 37
	v_cndmask_b32_e64 v70, 0, 1, vcc
	v_addc_co_u32_e64 v69, s[2:3], v69, v70, s[98:99]
	v_cmp_gt_i32_e32 vcc, s0, v0
	v_readlane_b32 s0, v0, 38
	v_cmp_gt_i32_e64 s[98:99], s1, v0
	v_readlane_b32 s1, v0, 39
	v_cndmask_b32_e64 v70, 0, 1, vcc
	v_addc_co_u32_e64 v69, s[2:3], v69, v70, s[98:99]
	v_cmp_gt_i32_e32 vcc, s0, v0
	v_readlane_b32 s0, v0, 40
	v_cmp_gt_i32_e64 s[98:99], s1, v0
	v_readlane_b32 s1, v0, 41
	v_cndmask_b32_e64 v70, 0, 1, vcc
	v_addc_co_u32_e64 v69, s[2:3], v69, v70, s[98:99]
	v_cmp_gt_i32_e32 vcc, s0, v0
	v_readlane_b32 s0, v0, 42
	v_cmp_gt_i32_e64 s[98:99], s1, v0
	v_readlane_b32 s1, v0, 43
	v_cndmask_b32_e64 v70, 0, 1, vcc
	v_addc_co_u32_e64 v69, s[2:3], v69, v70, s[98:99]
	v_cmp_gt_i32_e32 vcc, s0, v0
	v_readlane_b32 s0, v0, 44
	v_cmp_gt_i32_e64 s[98:99], s1, v0
	v_readlane_b32 s1, v0, 45
	v_cndmask_b32_e64 v70, 0, 1, vcc
	v_addc_co_u32_e64 v69, s[2:3], v69, v70, s[98:99]
	v_cmp_gt_i32_e32 vcc, s0, v0
	v_readlane_b32 s0, v0, 46
	v_cmp_gt_i32_e64 s[98:99], s1, v0
	v_readlane_b32 s1, v0, 47
	v_cndmask_b32_e64 v70, 0, 1, vcc
	v_addc_co_u32_e64 v69, s[2:3], v69, v70, s[98:99]
	v_cmp_gt_i32_e32 vcc, s0, v0
	v_readlane_b32 s0, v0, 48
	v_cmp_gt_i32_e64 s[98:99], s1, v0
	v_readlane_b32 s1, v0, 49
	v_cndmask_b32_e64 v70, 0, 1, vcc
	v_addc_co_u32_e64 v69, s[2:3], v69, v70, s[98:99]
	v_cmp_gt_i32_e32 vcc, s0, v0
	v_readlane_b32 s0, v0, 50
	v_cmp_gt_i32_e64 s[98:99], s1, v0
	v_readlane_b32 s1, v0, 51
	v_cndmask_b32_e64 v70, 0, 1, vcc
	v_addc_co_u32_e64 v69, s[2:3], v69, v70, s[98:99]
	v_cmp_gt_i32_e32 vcc, s0, v0
	v_readlane_b32 s0, v0, 52
	v_cmp_gt_i32_e64 s[98:99], s1, v0
	v_readlane_b32 s1, v0, 53
	v_cndmask_b32_e64 v70, 0, 1, vcc
	v_addc_co_u32_e64 v69, s[2:3], v69, v70, s[98:99]
	v_cmp_gt_i32_e32 vcc, s0, v0
	v_readlane_b32 s0, v0, 54
	v_cmp_gt_i32_e64 s[98:99], s1, v0
	v_readlane_b32 s1, v0, 55
	v_cndmask_b32_e64 v70, 0, 1, vcc
	v_addc_co_u32_e64 v69, s[2:3], v69, v70, s[98:99]
	v_cmp_gt_i32_e32 vcc, s0, v0
	v_readlane_b32 s0, v0, 56
	v_cmp_gt_i32_e64 s[98:99], s1, v0
	v_readlane_b32 s1, v0, 57
	v_cndmask_b32_e64 v70, 0, 1, vcc
	v_addc_co_u32_e64 v69, s[2:3], v69, v70, s[98:99]
	v_cmp_gt_i32_e32 vcc, s0, v0
	v_readlane_b32 s0, v0, 58
	v_cmp_gt_i32_e64 s[98:99], s1, v0
	v_readlane_b32 s1, v0, 59
	v_cndmask_b32_e64 v70, 0, 1, vcc
	v_addc_co_u32_e64 v69, s[2:3], v69, v70, s[98:99]
	v_cmp_gt_i32_e32 vcc, s0, v0
	v_readlane_b32 s0, v0, 60
	v_cmp_gt_i32_e64 s[98:99], s1, v0
	v_readlane_b32 s1, v0, 61
	v_cndmask_b32_e64 v70, 0, 1, vcc
	v_addc_co_u32_e64 v69, s[2:3], v69, v70, s[98:99]
	v_cmp_gt_i32_e32 vcc, s0, v0
	v_readlane_b32 s0, v0, 62
	v_cmp_gt_i32_e64 s[98:99], s1, v0
	v_readlane_b32 s1, v0, 63
	v_cndmask_b32_e64 v70, 0, 1, vcc
	v_addc_co_u32_e64 v69, s[2:3], v69, v70, s[98:99]
	v_cmp_gt_i32_e32 vcc, s0, v0
	v_cmp_gt_i32_e64 s[98:99], s1, v0
	s_nop 0
	v_cndmask_b32_e64 v70, 0, 1, vcc
	v_addc_co_u32_e64 v0, s[2:3], v69, v70, s[98:99]
	v_cmp_gt_u32_e64 s[2:3], 16, v0
	s_and_saveexec_b64 s[0:1], s[4:5]
	s_cbranch_execz .LBB0_676
	s_add_i32 s22, s29, s8
	v_mov_b32_e32 v0, s22
	v_mov_b64_e32 v[70:71], s[2:3]
	ds_write_b64 v0, v[70:71]
	s_branch .LBB0_676
	s_nop 0
	s_nop 0
	s_nop 0
	s_nop 0
	s_nop 0
	s_nop 0
	s_nop 0
	s_nop 0
	s_nop 0
	s_nop 0
	s_nop 0
	s_nop 0
	s_nop 0
	s_nop 0
	s_nop 0
